# v39 + nt on the P0 dense-weight conversion fp8 stores
# baseline (speedup 1.0000x reference)
.LBB0_43:
	ds_write2_b32 v165, v46, v47 offset1:1
	ds_write2_b32 v166, v48, v49 offset1:1
	ds_write2_b32 v167, v42, v43 offset1:1
	ds_write2_b32 v168, v44, v45 offset1:1
	ds_write2_b32 v169, v62, v63 offset1:1
	ds_write2_b32 v170, v64, v65 offset1:1
	ds_write2_b32 v171, v58, v59 offset1:1
	ds_write2_b32 v172, v60, v61 offset1:1
	ds_write2_b32 v173, v78, v79 offset1:1
	ds_write2_b32 v174, v80, v81 offset1:1
	ds_write2_b32 v175, v74, v75 offset1:1
	ds_write2_b32 v176, v76, v77 offset1:1
	ds_write2_b32 v177, v94, v95 offset1:1
	ds_write2_b32 v178, v96, v97 offset1:1
	ds_write2_b32 v179, v90, v91 offset1:1
	ds_write2_b32 v180, v92, v93 offset1:1
	ds_write2_b32 v181, v102, v103 offset1:1
	ds_write2_b32 v182, v104, v105 offset1:1
	ds_write2_b32 v183, v98, v99 offset1:1
	ds_write2_b32 v184, v100, v101 offset1:1
	ds_write2_b32 v185, v110, v111 offset1:1
	ds_write2_b32 v186, v112, v113 offset1:1
	ds_write2_b32 v187, v106, v107 offset1:1
	ds_write2_b32 v188, v108, v109 offset1:1
	ds_write2_b32 v189, v118, v119 offset1:1
	ds_write2_b32 v190, v120, v121 offset1:1
	ds_write2_b32 v191, v114, v115 offset1:1
	ds_write2_b32 v192, v116, v117 offset1:1
	ds_write2_b32 v193, v126, v127 offset1:1
	ds_write2_b32 v194, v128, v129 offset1:1
	ds_write2_b32 v195, v122, v123 offset1:1
	ds_write2_b32 v197, v124, v125 offset1:1
	s_waitcnt lgkmcnt(0)
	ds_read2_b32 v[166:167], v164 offset1:8
	ds_read2_b32 v[168:169], v164 offset0:65 offset1:73
	ds_read2_b32 v[170:171], v164 offset0:130 offset1:138
	ds_read2_b32 v[172:173], v164 offset0:195 offset1:203
	v_mov_b32_e32 v174, v133
	s_waitcnt lgkmcnt(3)
	v_mul_f32_e32 v132, 0x42000000, v166
	s_waitcnt lgkmcnt(2)
	v_mul_f32_e32 v152, 0x42000000, v168
	v_med3_f32 v132, v132, s26, v162
	v_med3_f32 v152, v152, s26, v162
	v_cvt_pk_fp8_f32 v174, v132, v152
	ds_read2_b32 v[176:177], v163 offset0:4 offset1:12
	ds_read2_b32 v[178:179], v163 offset0:69 offset1:77
	ds_read2_b32 v[180:181], v163 offset0:134 offset1:142
	s_waitcnt lgkmcnt(4)
	v_mul_f32_e32 v153, 0x42000000, v170
	s_waitcnt lgkmcnt(3)
	v_mul_f32_e32 v165, 0x42000000, v172
	v_med3_f32 v153, v153, s26, v162
	v_med3_f32 v132, v165, s26, v162
	ds_read2_b32 v[182:183], v163 offset0:199 offset1:207
	v_cvt_pk_fp8_f32 v174, v153, v132 op_sel:[0,0,1]
	s_waitcnt lgkmcnt(3)
	v_mul_f32_e32 v132, 0x42000000, v176
	s_waitcnt lgkmcnt(2)
	v_mul_f32_e32 v152, 0x42000000, v178
	v_med3_f32 v132, v132, s26, v162
	v_med3_f32 v152, v152, s26, v162
	v_mov_b32_e32 v175, v133
	v_cvt_pk_fp8_f32 v175, v132, v152
	s_waitcnt lgkmcnt(1)
	v_mul_f32_e32 v153, 0x42000000, v180
	s_waitcnt lgkmcnt(0)
	v_mul_f32_e32 v132, 0x42000000, v182
	v_med3_f32 v152, v153, s26, v162
	v_med3_f32 v132, v132, s26, v162
	v_cvt_pk_fp8_f32 v175, v152, v132 op_sel:[0,0,1]
	v_mul_f32_e32 v132, 0x42000000, v167
	v_mul_f32_e32 v165, 0x42000000, v169
	v_med3_f32 v132, v132, s26, v162
	v_med3_f32 v165, v165, s26, v162
	v_mov_b32_e32 v166, v133
	v_cvt_pk_fp8_f32 v166, v132, v165
	v_mul_f32_e32 v167, 0x42000000, v171
	v_mul_f32_e32 v132, 0x42000000, v173
	v_med3_f32 v165, v167, s26, v162
	v_med3_f32 v132, v132, s26, v162
	v_cvt_pk_fp8_f32 v166, v165, v132 op_sel:[0,0,1]
	v_mul_f32_e32 v132, 0x42000000, v177
	v_mul_f32_e32 v165, 0x42000000, v179
	v_med3_f32 v132, v132, s26, v162
	v_med3_f32 v165, v165, s26, v162
	v_mov_b32_e32 v167, v133
	v_mov_b64_e32 v[152:153], s[2:3]
	v_cvt_pk_fp8_f32 v167, v132, v165
	v_mad_u64_u32 v[184:185], s[6:7], s28, v134, v[152:153]
	v_lshl_add_u64 v[184:185], v[184:185], 0, v[136:137]
	v_mul_f32_e32 v168, 0x42000000, v181
	v_mul_f32_e32 v132, 0x42000000, v183
	global_store_dwordx2 v[184:185], v[174:175], off nt
	v_med3_f32 v165, v168, s26, v162
	v_med3_f32 v132, v132, s26, v162
	v_cvt_pk_fp8_f32 v167, v165, v132 op_sel:[0,0,1]
	ds_read2_b32 v[170:171], v164 offset0:16 offset1:24
	ds_read2_b32 v[172:173], v164 offset0:81 offset1:89
	ds_read2_b32 v[174:175], v164 offset0:146 offset1:154
	ds_read2_b32 v[176:177], v164 offset0:211 offset1:219
	v_mad_u64_u32 v[168:169], s[6:7], s28, v138, v[152:153]
	v_lshl_add_u64 v[168:169], v[168:169], 0, v[136:137]
	global_store_dwordx2 v[168:169], v[166:167], off nt
	s_waitcnt lgkmcnt(3)
	v_mul_f32_e32 v132, 0x42000000, v170
	s_waitcnt lgkmcnt(2)
	v_mul_f32_e32 v165, 0x42000000, v172
	s_waitcnt lgkmcnt(1)
	v_mul_f32_e32 v166, 0x42000000, v174
	v_med3_f32 v132, v132, s26, v162
	v_med3_f32 v165, v165, s26, v162
	v_med3_f32 v170, v166, s26, v162
	v_mov_b32_e32 v166, v133
	v_cvt_pk_fp8_f32 v166, v132, v165
	ds_read2_b32 v[168:169], v163 offset0:20 offset1:28
	ds_read2_b32 v[178:179], v163 offset0:85 offset1:93
	ds_read2_b32 v[180:181], v163 offset0:150 offset1:158
	s_waitcnt lgkmcnt(3)
	v_mul_f32_e32 v167, 0x42000000, v176
	v_med3_f32 v132, v167, s26, v162
	ds_read2_b32 v[182:183], v163 offset0:215 offset1:223
	v_cvt_pk_fp8_f32 v166, v170, v132 op_sel:[0,0,1]
	s_waitcnt lgkmcnt(3)
	v_mul_f32_e32 v132, 0x42000000, v168
	s_waitcnt lgkmcnt(2)
	v_mul_f32_e32 v165, 0x42000000, v178
	v_med3_f32 v132, v132, s26, v162
	v_med3_f32 v165, v165, s26, v162
	v_mov_b32_e32 v167, v133
	v_cvt_pk_fp8_f32 v167, v132, v165
	s_waitcnt lgkmcnt(1)
	v_mul_f32_e32 v168, 0x42000000, v180
	s_waitcnt lgkmcnt(0)
	v_mul_f32_e32 v132, 0x42000000, v182
	v_med3_f32 v165, v168, s26, v162
	v_med3_f32 v132, v132, s26, v162
	v_cvt_pk_fp8_f32 v167, v165, v132 op_sel:[0,0,1]
	v_mad_u64_u32 v[184:185], s[6:7], s28, v140, v[152:153]
	v_lshl_add_u64 v[184:185], v[184:185], 0, v[136:137]
	v_mul_f32_e32 v132, 0x42000000, v171
	v_mul_f32_e32 v165, 0x42000000, v173
	global_store_dwordx2 v[184:185], v[166:167], off nt
	v_med3_f32 v132, v132, s26, v162
	v_med3_f32 v165, v165, s26, v162
	v_mov_b32_e32 v166, v133
	v_cvt_pk_fp8_f32 v166, v132, v165
	v_mul_f32_e32 v167, 0x42000000, v175
	v_mul_f32_e32 v132, 0x42000000, v177
	v_med3_f32 v165, v167, s26, v162
	v_med3_f32 v132, v132, s26, v162
	v_cvt_pk_fp8_f32 v166, v165, v132 op_sel:[0,0,1]
	v_mul_f32_e32 v132, 0x42000000, v169
	v_mul_f32_e32 v165, 0x42000000, v179
	v_med3_f32 v132, v132, s26, v162
	v_med3_f32 v165, v165, s26, v162
	v_mov_b32_e32 v167, v133
	v_cvt_pk_fp8_f32 v167, v132, v165
	v_mul_f32_e32 v168, 0x42000000, v181
	v_mul_f32_e32 v132, 0x42000000, v183
	v_med3_f32 v165, v168, s26, v162
	v_med3_f32 v132, v132, s26, v162
	v_cvt_pk_fp8_f32 v167, v165, v132 op_sel:[0,0,1]
	ds_read2_b32 v[170:171], v164 offset0:32 offset1:40
	ds_read2_b32 v[172:173], v164 offset0:97 offset1:105
	ds_read2_b32 v[174:175], v164 offset0:162 offset1:170
	ds_read2_b32 v[176:177], v164 offset0:227 offset1:235
	v_mad_u64_u32 v[168:169], s[6:7], s28, v142, v[152:153]
	v_lshl_add_u64 v[168:169], v[168:169], 0, v[136:137]
	global_store_dwordx2 v[168:169], v[166:167], off nt
	s_waitcnt lgkmcnt(3)
	v_mul_f32_e32 v132, 0x42000000, v170
	s_waitcnt lgkmcnt(2)
	v_mul_f32_e32 v165, 0x42000000, v172
	s_waitcnt lgkmcnt(1)
	v_mul_f32_e32 v166, 0x42000000, v174
	v_med3_f32 v132, v132, s26, v162
	v_med3_f32 v165, v165, s26, v162
	v_med3_f32 v170, v166, s26, v162
	v_mov_b32_e32 v166, v133
	v_cvt_pk_fp8_f32 v166, v132, v165
	ds_read2_b32 v[168:169], v163 offset0:36 offset1:44
	ds_read2_b32 v[178:179], v163 offset0:101 offset1:109
	ds_read2_b32 v[180:181], v163 offset0:166 offset1:174
	s_waitcnt lgkmcnt(3)
	v_mul_f32_e32 v167, 0x42000000, v176
	v_med3_f32 v132, v167, s26, v162
	ds_read2_b32 v[182:183], v163 offset0:231 offset1:239
	v_cvt_pk_fp8_f32 v166, v170, v132 op_sel:[0,0,1]
	s_waitcnt lgkmcnt(3)
	v_mul_f32_e32 v132, 0x42000000, v168
	s_waitcnt lgkmcnt(2)
	v_mul_f32_e32 v165, 0x42000000, v178
	v_med3_f32 v132, v132, s26, v162
	v_med3_f32 v165, v165, s26, v162
	v_mov_b32_e32 v167, v133
	v_cvt_pk_fp8_f32 v167, v132, v165
	s_waitcnt lgkmcnt(1)
	v_mul_f32_e32 v168, 0x42000000, v180
	s_waitcnt lgkmcnt(0)
	v_mul_f32_e32 v132, 0x42000000, v182
	v_med3_f32 v165, v168, s26, v162
	v_med3_f32 v132, v132, s26, v162
	v_cvt_pk_fp8_f32 v167, v165, v132 op_sel:[0,0,1]
	v_mad_u64_u32 v[184:185], s[6:7], s28, v144, v[152:153]
	v_lshl_add_u64 v[184:185], v[184:185], 0, v[136:137]
	v_mul_f32_e32 v132, 0x42000000, v171
	v_mul_f32_e32 v165, 0x42000000, v173
	global_store_dwordx2 v[184:185], v[166:167], off nt
	v_med3_f32 v132, v132, s26, v162
	v_med3_f32 v165, v165, s26, v162
	v_mov_b32_e32 v166, v133
	v_cvt_pk_fp8_f32 v166, v132, v165
	v_mul_f32_e32 v167, 0x42000000, v175
	v_mul_f32_e32 v132, 0x42000000, v177
	v_med3_f32 v165, v167, s26, v162
	v_med3_f32 v132, v132, s26, v162
	v_cvt_pk_fp8_f32 v166, v165, v132 op_sel:[0,0,1]
	v_mul_f32_e32 v132, 0x42000000, v169
	v_mul_f32_e32 v165, 0x42000000, v179
	v_med3_f32 v132, v132, s26, v162
	v_med3_f32 v165, v165, s26, v162
	v_mov_b32_e32 v167, v133
	v_cvt_pk_fp8_f32 v167, v132, v165
	v_mul_f32_e32 v168, 0x42000000, v181
	v_mul_f32_e32 v132, 0x42000000, v183
	v_med3_f32 v165, v168, s26, v162
	v_med3_f32 v132, v132, s26, v162
	v_cvt_pk_fp8_f32 v167, v165, v132 op_sel:[0,0,1]
	ds_read2_b32 v[170:171], v164 offset0:48 offset1:56
	ds_read2_b32 v[172:173], v164 offset0:113 offset1:121
	ds_read2_b32 v[174:175], v164 offset0:178 offset1:186
	ds_read2_b32 v[164:165], v164 offset0:243 offset1:251
	v_mad_u64_u32 v[168:169], s[6:7], s28, v146, v[152:153]
	v_lshl_add_u64 v[168:169], v[168:169], 0, v[136:137]
	global_store_dwordx2 v[168:169], v[166:167], off nt
	s_waitcnt lgkmcnt(3)
	v_mul_f32_e32 v132, 0x42000000, v170
	s_waitcnt lgkmcnt(2)
	v_mul_f32_e32 v166, 0x42000000, v172
	v_med3_f32 v132, v132, s26, v162
	v_med3_f32 v168, v166, s26, v162
	v_mov_b32_e32 v166, v133
	v_cvt_pk_fp8_f32 v166, v132, v168
	ds_read2_b32 v[168:169], v163 offset0:52 offset1:60
	ds_read2_b32 v[176:177], v163 offset0:117 offset1:125
	ds_read2_b32 v[178:179], v163 offset0:182 offset1:190
	s_waitcnt lgkmcnt(4)
	v_mul_f32_e32 v167, 0x42000000, v174
	s_waitcnt lgkmcnt(3)
	v_mul_f32_e32 v164, 0x42000000, v164
	v_med3_f32 v167, v167, s26, v162
	v_med3_f32 v132, v164, s26, v162
	ds_read2_b32 v[180:181], v163 offset0:247 offset1:255
	v_cvt_pk_fp8_f32 v166, v167, v132 op_sel:[0,0,1]
	s_waitcnt lgkmcnt(3)
	v_mul_f32_e32 v132, 0x42000000, v168
	s_waitcnt lgkmcnt(2)
	v_mul_f32_e32 v164, 0x42000000, v176
	v_med3_f32 v132, v132, s26, v162
	v_med3_f32 v163, v164, s26, v162
	v_mov_b32_e32 v167, v133
	v_cvt_pk_fp8_f32 v167, v132, v163
	s_waitcnt lgkmcnt(1)
	v_mul_f32_e32 v168, 0x42000000, v178
	s_waitcnt lgkmcnt(0)
	v_mul_f32_e32 v132, 0x42000000, v180
	v_med3_f32 v163, v168, s26, v162
	v_med3_f32 v132, v132, s26, v162
	v_cvt_pk_fp8_f32 v167, v163, v132 op_sel:[0,0,1]
	v_mul_f32_e32 v132, 0x42000000, v171
	v_mul_f32_e32 v163, 0x42000000, v173
	v_med3_f32 v132, v132, s26, v162
	v_med3_f32 v163, v163, s26, v162
	v_mov_b32_e32 v164, v133
	v_mad_u64_u32 v[182:183], s[6:7], s28, v148, v[152:153]
	v_cvt_pk_fp8_f32 v164, v132, v163
	v_lshl_add_u64 v[182:183], v[182:183], 0, v[136:137]
	global_store_dwordx2 v[182:183], v[166:167], off nt
	v_mul_f32_e32 v166, 0x42000000, v175
	v_mul_f32_e32 v132, 0x42000000, v165
	v_med3_f32 v163, v166, s26, v162
	v_med3_f32 v132, v132, s26, v162
	v_cvt_pk_fp8_f32 v164, v163, v132 op_sel:[0,0,1]
	v_mul_f32_e32 v132, 0x42000000, v169
	v_mul_f32_e32 v163, 0x42000000, v177
	v_med3_f32 v132, v132, s26, v162
	v_med3_f32 v163, v163, s26, v162
	v_mov_b32_e32 v165, v133
	v_cvt_pk_fp8_f32 v165, v132, v163
	v_mul_f32_e32 v166, 0x42000000, v179
	v_mul_f32_e32 v132, 0x42000000, v181
	v_med3_f32 v163, v166, s26, v162
	v_med3_f32 v132, v132, s26, v162
	v_cvt_pk_fp8_f32 v165, v163, v132 op_sel:[0,0,1]
	v_mad_u64_u32 v[152:153], s[6:7], s28, v150, v[152:153]
	v_lshl_add_u64 v[152:153], v[152:153], 0, v[136:137]
	global_store_dwordx2 v[152:153], v[164:165], off nt
	s_waitcnt lgkmcnt(0)

.LBB0_59:
	v_add_u32_e32 v165, 0x4000, v161
	v_add_u32_e32 v166, 0x4008, v161
	v_add_u32_e32 v167, 0x4410, v161
	v_add_u32_e32 v168, 0x4418, v161
	v_add_u32_e32 v169, 0x4820, v161
	v_add_u32_e32 v170, 0x4828, v161
	v_add_u32_e32 v171, 0x4c30, v161
	v_add_u32_e32 v172, 0x4c38, v161
	v_add_u32_e32 v173, 0x5040, v161
	v_add_u32_e32 v174, 0x5048, v161
	v_add_u32_e32 v175, 0x5450, v161
	v_add_u32_e32 v176, 0x5458, v161
	v_add_u32_e32 v177, 0x5860, v161
	v_add_u32_e32 v178, 0x5868, v161
	v_add_u32_e32 v179, 0x5c70, v161
	v_add_u32_e32 v180, 0x5c78, v161
	v_add_u32_e32 v181, 0x6080, v161
	v_add_u32_e32 v182, 0x6088, v161
	v_add_u32_e32 v183, 0x6490, v161
	v_add_u32_e32 v184, 0x6498, v161
	v_add_u32_e32 v185, 0x68a0, v161
	v_add_u32_e32 v186, 0x68a8, v161
	v_add_u32_e32 v187, 0x6cb0, v161
	v_add_u32_e32 v188, 0x6cb8, v161
	v_add_u32_e32 v189, 0x70c0, v161
	v_add_u32_e32 v190, 0x70c8, v161
	v_add_u32_e32 v191, 0x74d0, v161
	v_add_u32_e32 v192, 0x74d8, v161
	v_add_u32_e32 v193, 0x78e0, v161
	v_add_u32_e32 v194, 0x78e8, v161
	v_add_u32_e32 v195, 0x7cf0, v161
	v_add_u32_e32 v197, 0x7cf8, v161
	s_waitcnt vmcnt(15)
	ds_write2_b32 v165, v2, v3 offset1:1
	ds_write2_b32 v166, v4, v5 offset1:1
	s_waitcnt vmcnt(14)
	ds_write2_b32 v167, v6, v7 offset1:1
	ds_write2_b32 v168, v8, v9 offset1:1
	s_waitcnt vmcnt(13)
	ds_write2_b32 v169, v10, v11 offset1:1
	ds_write2_b32 v170, v12, v13 offset1:1
	s_waitcnt vmcnt(12)
	ds_write2_b32 v171, v14, v15 offset1:1
	ds_write2_b32 v172, v16, v17 offset1:1
	s_waitcnt vmcnt(11)
	ds_write2_b32 v173, v18, v19 offset1:1
	ds_write2_b32 v174, v20, v21 offset1:1
	s_waitcnt vmcnt(10)
	ds_write2_b32 v175, v22, v23 offset1:1
	ds_write2_b32 v176, v24, v25 offset1:1
	s_waitcnt vmcnt(9)
	ds_write2_b32 v177, v26, v27 offset1:1
	ds_write2_b32 v178, v28, v29 offset1:1
	s_waitcnt vmcnt(8)
	ds_write2_b32 v179, v30, v31 offset1:1
	ds_write2_b32 v180, v32, v33 offset1:1
	s_waitcnt vmcnt(7)
	ds_write2_b32 v181, v34, v35 offset1:1
	ds_write2_b32 v182, v36, v37 offset1:1
	s_waitcnt vmcnt(6)
	ds_write2_b32 v183, v38, v39 offset1:1
	ds_write2_b32 v184, v40, v41 offset1:1
	s_waitcnt vmcnt(5)
	ds_write2_b32 v185, v50, v51 offset1:1
	ds_write2_b32 v186, v52, v53 offset1:1
	s_waitcnt vmcnt(4)
	ds_write2_b32 v187, v54, v55 offset1:1
	ds_write2_b32 v188, v56, v57 offset1:1
	s_waitcnt vmcnt(3)
	ds_write2_b32 v189, v66, v67 offset1:1
	ds_write2_b32 v190, v68, v69 offset1:1
	s_waitcnt vmcnt(2)
	ds_write2_b32 v191, v70, v71 offset1:1
	ds_write2_b32 v192, v72, v73 offset1:1
	s_waitcnt vmcnt(1)
	ds_write2_b32 v193, v82, v83 offset1:1
	ds_write2_b32 v194, v84, v85 offset1:1
	s_waitcnt vmcnt(0)
	ds_write2_b32 v195, v86, v87 offset1:1
	ds_write2_b32 v197, v88, v89 offset1:1
	s_waitcnt lgkmcnt(0)
	v_add_u32_e32 v164, 0x4000, v160
	ds_read2_b32 v[198:199], v164 offset1:8
	ds_read2_b32 v[200:201], v164 offset0:65 offset1:73
	ds_read2_b32 v[202:203], v164 offset0:130 offset1:138
	ds_read2_b32 v[204:205], v164 offset0:195 offset1:203
	v_mov_b32_e32 v206, v133
	s_waitcnt lgkmcnt(3)
	v_mul_f32_e32 v132, 0x42000000, v198
	s_waitcnt lgkmcnt(2)
	v_mul_f32_e32 v152, 0x42000000, v200
	v_med3_f32 v132, v132, s26, v162
	v_med3_f32 v152, v152, s26, v162
	v_add_u32_e32 v163, 0x4400, v160
	v_cvt_pk_fp8_f32 v206, v132, v152
	ds_read2_b32 v[208:209], v163 offset0:4 offset1:12
	ds_read2_b32 v[210:211], v163 offset0:69 offset1:77
	ds_read2_b32 v[212:213], v163 offset0:134 offset1:142
	s_waitcnt lgkmcnt(4)
	v_mul_f32_e32 v153, 0x42000000, v202
	s_waitcnt lgkmcnt(3)
	v_mul_f32_e32 v198, 0x42000000, v204
	v_med3_f32 v153, v153, s26, v162
	v_med3_f32 v132, v198, s26, v162
	ds_read2_b32 v[214:215], v163 offset0:199 offset1:207
	v_cvt_pk_fp8_f32 v206, v153, v132 op_sel:[0,0,1]
	s_waitcnt lgkmcnt(3)
	v_mul_f32_e32 v132, 0x42000000, v208
	s_waitcnt lgkmcnt(2)
	v_mul_f32_e32 v152, 0x42000000, v210
	v_med3_f32 v132, v132, s26, v162
	v_med3_f32 v152, v152, s26, v162
	v_mov_b32_e32 v207, v133
	v_cvt_pk_fp8_f32 v207, v132, v152
	s_waitcnt lgkmcnt(1)
	v_mul_f32_e32 v153, 0x42000000, v212
	s_waitcnt lgkmcnt(0)
	v_mul_f32_e32 v132, 0x42000000, v214
	v_med3_f32 v152, v153, s26, v162
	v_med3_f32 v132, v132, s26, v162
	v_cvt_pk_fp8_f32 v207, v152, v132 op_sel:[0,0,1]
	v_mul_f32_e32 v132, 0x42000000, v199
	v_mul_f32_e32 v198, 0x42000000, v201
	v_med3_f32 v132, v132, s26, v162
	v_med3_f32 v200, v198, s26, v162
	v_mov_b32_e32 v198, v133
	v_cvt_pk_fp8_f32 v198, v132, v200
	v_mul_f32_e32 v199, 0x42000000, v203
	v_mul_f32_e32 v132, 0x42000000, v205
	v_med3_f32 v199, v199, s26, v162
	v_med3_f32 v132, v132, s26, v162
	v_cvt_pk_fp8_f32 v198, v199, v132 op_sel:[0,0,1]
	v_mul_f32_e32 v132, 0x42000000, v209
	v_mul_f32_e32 v199, 0x42000000, v211
	v_med3_f32 v132, v132, s26, v162
	v_med3_f32 v201, v199, s26, v162
	v_mov_b32_e32 v199, v133
	v_cvt_pk_fp8_f32 v199, v132, v201
	v_mov_b64_e32 v[152:153], s[0:1]
	v_mad_u64_u32 v[216:217], s[6:7], s10, v134, v[152:153]
	v_mul_f32_e32 v200, 0x42000000, v213
	v_mul_f32_e32 v132, 0x42000000, v215
	v_lshl_add_u64 v[216:217], v[216:217], 0, v[136:137]
	v_med3_f32 v200, v200, s26, v162
	v_med3_f32 v132, v132, s26, v162
	global_store_dwordx2 v[216:217], v[206:207], off nt
	v_cvt_pk_fp8_f32 v199, v200, v132 op_sel:[0,0,1]
	ds_read2_b32 v[202:203], v164 offset0:16 offset1:24
	ds_read2_b32 v[204:205], v164 offset0:81 offset1:89
	ds_read2_b32 v[206:207], v164 offset0:146 offset1:154
	ds_read2_b32 v[208:209], v164 offset0:211 offset1:219
	v_mad_u64_u32 v[200:201], s[6:7], s10, v138, v[152:153]
	v_lshl_add_u64 v[200:201], v[200:201], 0, v[136:137]
	global_store_dwordx2 v[200:201], v[198:199], off nt
	s_waitcnt lgkmcnt(3)
	v_mul_f32_e32 v132, 0x42000000, v202
	s_waitcnt lgkmcnt(2)
	v_mul_f32_e32 v198, 0x42000000, v204
	v_med3_f32 v132, v132, s26, v162
	v_med3_f32 v200, v198, s26, v162
	v_mov_b32_e32 v198, v133
	v_cvt_pk_fp8_f32 v198, v132, v200
	ds_read2_b32 v[200:201], v163 offset0:20 offset1:28
	ds_read2_b32 v[210:211], v163 offset0:85 offset1:93
	ds_read2_b32 v[212:213], v163 offset0:150 offset1:158
	s_waitcnt lgkmcnt(4)
	v_mul_f32_e32 v199, 0x42000000, v206
	s_waitcnt lgkmcnt(3)
	v_mul_f32_e32 v202, 0x42000000, v208
	v_med3_f32 v199, v199, s26, v162
	v_med3_f32 v132, v202, s26, v162
	ds_read2_b32 v[214:215], v163 offset0:215 offset1:223
	v_cvt_pk_fp8_f32 v198, v199, v132 op_sel:[0,0,1]
	s_waitcnt lgkmcnt(3)
	v_mul_f32_e32 v132, 0x42000000, v200
	s_waitcnt lgkmcnt(2)
	v_mul_f32_e32 v199, 0x42000000, v210
	v_med3_f32 v132, v132, s26, v162
	v_med3_f32 v202, v199, s26, v162
	v_mov_b32_e32 v199, v133
	v_cvt_pk_fp8_f32 v199, v132, v202
	s_waitcnt lgkmcnt(1)
	v_mul_f32_e32 v200, 0x42000000, v212
	s_waitcnt lgkmcnt(0)
	v_mul_f32_e32 v132, 0x42000000, v214
	v_med3_f32 v200, v200, s26, v162
	v_med3_f32 v132, v132, s26, v162
	v_cvt_pk_fp8_f32 v199, v200, v132 op_sel:[0,0,1]
	v_mad_u64_u32 v[216:217], s[6:7], s10, v140, v[152:153]
	v_lshl_add_u64 v[216:217], v[216:217], 0, v[136:137]
	global_store_dwordx2 v[216:217], v[198:199], off nt
	v_mul_f32_e32 v132, 0x42000000, v203
	v_mul_f32_e32 v198, 0x42000000, v205
	v_med3_f32 v132, v132, s26, v162
	v_med3_f32 v200, v198, s26, v162
	v_mov_b32_e32 v198, v133
	v_cvt_pk_fp8_f32 v198, v132, v200
	v_mul_f32_e32 v199, 0x42000000, v207
	v_mul_f32_e32 v132, 0x42000000, v209
	v_med3_f32 v199, v199, s26, v162
	v_med3_f32 v132, v132, s26, v162
	v_cvt_pk_fp8_f32 v198, v199, v132 op_sel:[0,0,1]
	v_mul_f32_e32 v132, 0x42000000, v201
	v_mul_f32_e32 v199, 0x42000000, v211
	v_med3_f32 v132, v132, s26, v162
	v_med3_f32 v201, v199, s26, v162
	v_mov_b32_e32 v199, v133
	v_cvt_pk_fp8_f32 v199, v132, v201
	v_mul_f32_e32 v200, 0x42000000, v213
	v_mul_f32_e32 v132, 0x42000000, v215
	v_med3_f32 v200, v200, s26, v162
	v_med3_f32 v132, v132, s26, v162
	v_cvt_pk_fp8_f32 v199, v200, v132 op_sel:[0,0,1]
	ds_read2_b32 v[202:203], v164 offset0:32 offset1:40
	ds_read2_b32 v[204:205], v164 offset0:97 offset1:105
	ds_read2_b32 v[206:207], v164 offset0:162 offset1:170
	ds_read2_b32 v[208:209], v164 offset0:227 offset1:235
	v_mad_u64_u32 v[200:201], s[6:7], s10, v142, v[152:153]
	v_lshl_add_u64 v[200:201], v[200:201], 0, v[136:137]
	global_store_dwordx2 v[200:201], v[198:199], off nt
	s_waitcnt lgkmcnt(3)
	v_mul_f32_e32 v132, 0x42000000, v202
	s_waitcnt lgkmcnt(2)
	v_mul_f32_e32 v198, 0x42000000, v204
	v_med3_f32 v132, v132, s26, v162
	v_med3_f32 v200, v198, s26, v162
	v_mov_b32_e32 v198, v133
	v_cvt_pk_fp8_f32 v198, v132, v200
	ds_read2_b32 v[200:201], v163 offset0:36 offset1:44
	ds_read2_b32 v[210:211], v163 offset0:101 offset1:109
	ds_read2_b32 v[212:213], v163 offset0:166 offset1:174
	s_waitcnt lgkmcnt(4)
	v_mul_f32_e32 v199, 0x42000000, v206
	s_waitcnt lgkmcnt(3)
	v_mul_f32_e32 v202, 0x42000000, v208
	v_med3_f32 v199, v199, s26, v162
	v_med3_f32 v132, v202, s26, v162
	ds_read2_b32 v[214:215], v163 offset0:231 offset1:239
	v_cvt_pk_fp8_f32 v198, v199, v132 op_sel:[0,0,1]
	s_waitcnt lgkmcnt(3)
	v_mul_f32_e32 v132, 0x42000000, v200
	s_waitcnt lgkmcnt(2)
	v_mul_f32_e32 v199, 0x42000000, v210
	v_med3_f32 v132, v132, s26, v162
	v_med3_f32 v202, v199, s26, v162
	v_mov_b32_e32 v199, v133
	v_cvt_pk_fp8_f32 v199, v132, v202
	s_waitcnt lgkmcnt(1)
	v_mul_f32_e32 v200, 0x42000000, v212
	s_waitcnt lgkmcnt(0)
	v_mul_f32_e32 v132, 0x42000000, v214
	v_med3_f32 v200, v200, s26, v162
	v_med3_f32 v132, v132, s26, v162
	v_cvt_pk_fp8_f32 v199, v200, v132 op_sel:[0,0,1]
	v_mad_u64_u32 v[216:217], s[6:7], s10, v144, v[152:153]
	v_lshl_add_u64 v[216:217], v[216:217], 0, v[136:137]
	global_store_dwordx2 v[216:217], v[198:199], off nt
	v_mul_f32_e32 v132, 0x42000000, v203
	v_mul_f32_e32 v198, 0x42000000, v205
	v_med3_f32 v132, v132, s26, v162
	v_med3_f32 v200, v198, s26, v162
	v_mov_b32_e32 v198, v133
	v_cvt_pk_fp8_f32 v198, v132, v200
	v_mul_f32_e32 v199, 0x42000000, v207
	v_mul_f32_e32 v132, 0x42000000, v209
	v_med3_f32 v199, v199, s26, v162
	v_med3_f32 v132, v132, s26, v162
	v_cvt_pk_fp8_f32 v198, v199, v132 op_sel:[0,0,1]
	v_mul_f32_e32 v132, 0x42000000, v201
	v_mul_f32_e32 v199, 0x42000000, v211
	v_med3_f32 v132, v132, s26, v162
	v_med3_f32 v201, v199, s26, v162
	v_mov_b32_e32 v199, v133
	v_cvt_pk_fp8_f32 v199, v132, v201
	v_mul_f32_e32 v200, 0x42000000, v213
	v_mul_f32_e32 v132, 0x42000000, v215
	v_med3_f32 v200, v200, s26, v162
	v_med3_f32 v132, v132, s26, v162
	v_cvt_pk_fp8_f32 v199, v200, v132 op_sel:[0,0,1]
	ds_read2_b32 v[202:203], v164 offset0:48 offset1:56
	ds_read2_b32 v[204:205], v164 offset0:113 offset1:121
	ds_read2_b32 v[206:207], v164 offset0:178 offset1:186
	ds_read2_b32 v[208:209], v164 offset0:243 offset1:251
	v_mad_u64_u32 v[200:201], s[6:7], s10, v146, v[152:153]
	v_lshl_add_u64 v[200:201], v[200:201], 0, v[136:137]
	global_store_dwordx2 v[200:201], v[198:199], off nt
	s_waitcnt lgkmcnt(3)
	v_mul_f32_e32 v132, 0x42000000, v202
	s_waitcnt lgkmcnt(2)
	v_mul_f32_e32 v198, 0x42000000, v204
	v_med3_f32 v132, v132, s26, v162
	v_med3_f32 v200, v198, s26, v162
	v_mov_b32_e32 v198, v133
	v_cvt_pk_fp8_f32 v198, v132, v200
	ds_read2_b32 v[200:201], v163 offset0:52 offset1:60
	ds_read2_b32 v[210:211], v163 offset0:117 offset1:125
	ds_read2_b32 v[212:213], v163 offset0:182 offset1:190
	s_waitcnt lgkmcnt(4)
	v_mul_f32_e32 v199, 0x42000000, v206
	s_waitcnt lgkmcnt(3)
	v_mul_f32_e32 v202, 0x42000000, v208
	v_med3_f32 v199, v199, s26, v162
	v_med3_f32 v132, v202, s26, v162
	ds_read2_b32 v[214:215], v163 offset0:247 offset1:255
	v_cvt_pk_fp8_f32 v198, v199, v132 op_sel:[0,0,1]
	s_waitcnt lgkmcnt(3)
	v_mul_f32_e32 v132, 0x42000000, v200
	s_waitcnt lgkmcnt(2)
	v_mul_f32_e32 v199, 0x42000000, v210
	v_med3_f32 v132, v132, s26, v162
	v_med3_f32 v202, v199, s26, v162
	v_mov_b32_e32 v199, v133
	v_cvt_pk_fp8_f32 v199, v132, v202
	s_waitcnt lgkmcnt(1)
	v_mul_f32_e32 v200, 0x42000000, v212
	s_waitcnt lgkmcnt(0)
	v_mul_f32_e32 v132, 0x42000000, v214
	v_med3_f32 v200, v200, s26, v162
	v_med3_f32 v132, v132, s26, v162
	v_cvt_pk_fp8_f32 v199, v200, v132 op_sel:[0,0,1]
	v_mad_u64_u32 v[216:217], s[6:7], s10, v148, v[152:153]
	v_lshl_add_u64 v[216:217], v[216:217], 0, v[136:137]
	global_store_dwordx2 v[216:217], v[198:199], off nt
	v_mul_f32_e32 v132, 0x42000000, v203
	v_mul_f32_e32 v198, 0x42000000, v205
	v_med3_f32 v132, v132, s26, v162
	v_med3_f32 v200, v198, s26, v162
	v_mov_b32_e32 v198, v133
	v_cvt_pk_fp8_f32 v198, v132, v200
	v_mul_f32_e32 v199, 0x42000000, v207
	v_mul_f32_e32 v132, 0x42000000, v209
	v_med3_f32 v199, v199, s26, v162
	v_med3_f32 v132, v132, s26, v162
	v_cvt_pk_fp8_f32 v198, v199, v132 op_sel:[0,0,1]
	v_mul_f32_e32 v132, 0x42000000, v201
	v_mul_f32_e32 v199, 0x42000000, v211
	v_med3_f32 v132, v132, s26, v162
	v_med3_f32 v201, v199, s26, v162
	v_mov_b32_e32 v199, v133
	v_cvt_pk_fp8_f32 v199, v132, v201
	v_mul_f32_e32 v200, 0x42000000, v213
	v_mul_f32_e32 v132, 0x42000000, v215
	v_med3_f32 v200, v200, s26, v162
	v_med3_f32 v132, v132, s26, v162
	v_cvt_pk_fp8_f32 v199, v200, v132 op_sel:[0,0,1]
	v_mad_u64_u32 v[152:153], s[6:7], s10, v150, v[152:153]
	v_lshl_add_u64 v[152:153], v[152:153], 0, v[136:137]
	global_store_dwordx2 v[152:153], v[198:199], off nt
	s_waitcnt lgkmcnt(0)
	s_andn2_b64 vcc, exec, s[4:5]
	s_mov_b64 s[4:5], -1
	s_cbranch_vccnz .LBB0_44
	s_add_i32 s30, s29, s11
	s_cmpk_gt_i32 s30, 0x2fff
	s_cselect_b64 s[4:5], -1, 0
	s_and_b64 vcc, exec, s[4:5]
	s_cbranch_vccnz .LBB0_43
	s_cmpk_gt_i32 s30, 0x25ff
	s_mov_b64 s[8:9], -1
	s_cbranch_scc0 .LBB0_71
	s_lshr_b32 s0, s30, 2
	s_and_b32 s0, s0, 30
	s_and_b32 s1, s27, 1
	s_bfe_u32 s31, s27, 0x20001
	s_or_b32 s29, s0, s1
	s_cmpk_gt_u32 s30, 0x27ff
	s_cbranch_scc0 .LBB0_68
	s_lshr_b32 s0, s30, 5
	s_and_b32 s0, s0, 60
	s_or_b32 s0, s0, s31
	s_lshl_b32 s10, s0, 6
	s_cmpk_gt_u32 s30, 0x2bff
	s_cbranch_scc0 .LBB0_65
	v_mov_b32_e32 v2, s22
	ds_read_b64 v[2:3], v2
	s_xor_b32 s0, s10, 0x800
	s_lshl_b32 s1, s0, 13
	s_waitcnt lgkmcnt(0)
	v_readfirstlane_b32 s6, v2
	v_readfirstlane_b32 s7, v3
	s_add_u32 s1, s6, s1
	s_addc_u32 s7, s7, 0
	s_lshl_b32 s6, s29, 8
	s_add_u32 s6, s1, s6
	s_addc_u32 s7, s7, 0
	s_lshl_b32 s1, s29, 17
	s_add_u32 s1, s12, s1
	s_addc_u32 s8, s13, 0
	s_add_u32 s0, s1, s0
	s_addc_u32 s1, s8, 0
	s_mov_b64 s[8:9], 0
